# speedup vs baseline: 1.0055x; 1.0055x over previous
_Z9gemm_gldsILi256ELi192ELi4ELi2ELi2ELi4ELi8ELi0ELi4096ELi3072ELi1024EEvPKDF16_S1_PfPKfS4_PKiPDF16_S7_S7_:
	s_mov_b32 s47, s2
	s_ashr_i32 s3, s2, 3
	s_lshr_b32 s9, s3, 30
	s_add_i32 s9, s3, s9
	s_lshl_b32 s8, s2, 1
	s_ashr_i32 s10, s9, 2
	s_and_b32 s9, s9, 0xfffffc
	s_lshl_b32 s2, s2, 3
	s_load_dwordx4 s[4:7], s[0:1], 0x0
	s_and_b32 s8, s8, 12
	s_sub_i32 s3, s3, s9
	s_and_b32 s20, s2, 8
	s_add_i32 s8, s8, s3
	s_add_i32 s20, s20, s10
	s_lshl_b32 s16, s8, 8
	s_mul_i32 s2, s20, 0xc0
	v_lshlrev_b32_e32 v139, 4, v0
	v_and_b32_e32 v1, 32, v0
	s_ashr_i32 s17, s16, 31
	s_ashr_i32 s3, s2, 31
	v_lshrrev_b32_e32 v2, 3, v0
	v_bfe_u32 v46, v0, 2, 4
	v_bitop3_b32 v1, v139, v1, 48 bitop3:0x6c
	s_lshl_b64 s[8:9], s[16:17], 11
	s_lshl_b64 s[10:11], s[2:3], 11
	v_and_or_b32 v2, v2, 48, v46
	v_and_or_b32 v47, v0, 64, v1
	s_waitcnt lgkmcnt(0)
	s_add_u32 s50, s4, 0x3082000
	s_addc_u32 s51, s5, 0
	s_load_dwordx2 s[52:53], s[50:51], 0x0
	s_add_u32 s54, s4, 0x3000000
	s_addc_u32 s55, s5, 0
	s_add_u32 s56, s4, 0x3080000
	s_addc_u32 s57, s5, 0
	s_add_u32 s2, s4, s8
	s_addc_u32 s3, s5, s9
	v_lshl_or_b32 v2, v2, 11, v47
	v_mov_b32_e32 v3, 0
	v_readfirstlane_b32 s4, v139
	v_or_b32_e32 v1, 0x2000, v139
	s_add_u32 s18, s6, s10
	v_lshl_add_u64 v[4:5], s[2:3], 0, v[2:3]
	s_mov_b32 m0, s4
	s_mov_b64 s[4:5], 0x20000
	v_readfirstlane_b32 s6, v1
	v_or_b32_e32 v1, 0x4000, v139
	s_addc_u32 s19, s7, s11
	global_load_lds_dwordx4 v2, s[2:3]
	v_lshl_add_u64 v[8:9], v[4:5], 0, s[4:5]
	s_mov_b32 m0, s6
	s_mov_b64 s[6:7], 0x40000
	v_readfirstlane_b32 s8, v1
	global_load_lds_dwordx4 v[8:9], off
	v_lshl_add_u64 v[8:9], v[4:5], 0, s[6:7]
	s_mov_b32 m0, s8
	s_mov_b64 s[8:9], 0x60000
	v_or_b32_e32 v1, 0x6000, v139
	global_load_lds_dwordx4 v[8:9], off
	v_lshl_add_u64 v[8:9], v[4:5], 0, s[8:9]
	v_readfirstlane_b32 s8, v1
	v_or_b32_e32 v1, 0x8000, v139
	v_lshl_add_u64 v[6:7], s[18:19], 0, v[2:3]
	s_mov_b32 m0, s8
	v_readfirstlane_b32 s8, v1
	v_or_b32_e32 v1, 0xa000, v139
	global_load_lds_dwordx4 v[8:9], off
	s_mov_b32 m0, s8
	v_lshl_add_u64 v[8:9], v[6:7], 0, s[4:5]
	v_readfirstlane_b32 s4, v1
	v_or_b32_e32 v1, 0xc000, v139
	global_load_lds_dwordx4 v2, s[18:19]
	s_mov_b32 m0, s4
	v_readfirstlane_b32 s4, v1
	v_or_b32_e32 v1, 0xe000, v139
	global_load_lds_dwordx4 v[8:9], off
	v_lshl_add_u64 v[8:9], v[6:7], 0, s[6:7]
	s_mov_b32 m0, s4
	s_mov_b64 s[4:5], 0x80
	v_readfirstlane_b32 s6, v1
	v_or_b32_e32 v1, 0x10000, v139
	global_load_lds_dwordx4 v[8:9], off
	v_lshl_add_u64 v[8:9], v[4:5], 0, s[4:5]
	s_mov_b32 m0, s6
	s_mov_b64 s[6:7], 0x20080
	v_readfirstlane_b32 s8, v1
	v_or_b32_e32 v1, 0x12000, v139
	global_load_lds_dwordx4 v[8:9], off
	v_lshl_add_u64 v[8:9], v[4:5], 0, s[6:7]
	s_mov_b32 m0, s8
	v_readfirstlane_b32 s10, v1
	global_load_lds_dwordx4 v[8:9], off
	s_mov_b64 s[8:9], 0x40080
	s_mov_b32 m0, s10
	s_mov_b64 s[10:11], 0x60080
	v_or_b32_e32 v1, 0x14000, v139
	v_lshl_add_u64 v[8:9], v[4:5], 0, s[8:9]
	v_lshl_add_u64 v[4:5], v[4:5], 0, s[10:11]
	v_readfirstlane_b32 s10, v1
	global_load_lds_dwordx4 v[8:9], off
	s_mov_b32 m0, s10
	v_or_b32_e32 v1, 0x16000, v139
	global_load_lds_dwordx4 v[4:5], off
	v_lshl_add_u64 v[4:5], v[6:7], 0, s[4:5]
	v_readfirstlane_b32 s4, v1
	v_or_b32_e32 v1, 0x18000, v139
	s_mov_b32 m0, s4
	v_readfirstlane_b32 s4, v1
	v_or_b32_e32 v1, 0x1a000, v139
	global_load_lds_dwordx4 v[4:5], off
	v_lshl_add_u64 v[4:5], v[6:7], 0, s[6:7]
	s_mov_b32 m0, s4
	v_readfirstlane_b32 s4, v1
	global_load_lds_dwordx4 v[4:5], off
	v_lshl_add_u64 v[4:5], v[6:7], 0, s[8:9]
	s_mov_b32 m0, s4
	v_lshrrev_b32_e32 v2, 7, v0
	global_load_lds_dwordx4 v[4:5], off
	s_load_dwordx4 s[12:15], s[0:1], 0x38
	s_load_dwordx8 s[4:11], s[0:1], 0x18
	v_lshlrev_b32_e32 v4, 6, v0
	v_and_b32_e32 v138, 48, v0
	v_and_b32_e32 v4, 0x3c0, v4
	v_lshlrev_b32_e32 v6, 2, v0
	v_bfe_u32 v144, v0, 6, 1
	v_or_b32_e32 v14, v4, v138
	v_lshlrev_b32_e32 v5, 13, v2
	v_and_b32_e32 v15, 32, v6
	v_and_b32_e32 v1, 15, v0
	v_bitop3_b32 v151, v4, v15, v138 bitop3:0x36
	v_bitop3_b32 v146, v5, v14, v15 bitop3:0xf6
	v_mul_u32_u24_e32 v152, 0x3000, v144
	v_lshl_or_b32 v145, v2, 6, s16
	v_or_b32_e32 v4, v145, v1
	v_ashrrev_i32_e32 v5, 31, v4
	s_waitcnt lgkmcnt(0)
	v_lshl_add_u64 v[4:5], v[4:5], 2, s[8:9]
	global_load_dword v150, v[4:5], off
	global_load_dword v149, v[4:5], off offset:64
	global_load_dword v148, v[4:5], off offset:128
	global_load_dword v147, v[4:5], off offset:192
	v_readfirstlane_b32 s48, v0
	v_and_b32_e32 v248, 63, v0
	v_lshlrev_b32_e32 v248, 2, v248
	s_lshr_b32 s48, s48, 6
	s_and_b32 s49, s48, 1
	s_lshr_b32 s48, s48, 1
	s_lshr_b32 s58, s47, 3
	s_lshl_b32 s58, s58, 6
	s_lshl_b32 s61, s49, 5
	s_add_u32 s58, s58, s61
	s_and_b32 s59, s47, 7
	s_lshl_b32 s59, s59, 2
	s_add_u32 s59, s59, s48
	s_lshl_b32 s60, s47, 2
	s_add_u32 s60, s60, s48
	s_lshl_b32 s60, s60, 2
	s_lshl_b32 s61, s49, 1
	s_add_u32 s60, s60, s61
	s_lshl_b32 s61, s58, 13
	s_lshl_b32 s62, s59, 8
	s_add_u32 s61, s61, s62
	s_add_u32 s66, s52, s61
	s_addc_u32 s67, s53, 0
	v_bitop3_b32 v153, v152, v14, v15 bitop3:0xf6
	s_waitcnt vmcnt(7) lgkmcnt(0)
	s_barrier
	ds_read_b128 v[42:45], v146
	ds_read_b128 v[38:41], v146 offset:2048
	ds_read_b128 v[10:13], v146 offset:4096
	ds_read_b128 v[6:9], v146 offset:6144
	ds_read_b128 v[22:25], v153 offset:32768
	ds_read_b128 v[18:21], v153 offset:34816
	ds_read_b128 v[30:33], v153 offset:36864
	ds_read_b128 v[26:29], v153 offset:38912
	ds_read_b128 v[34:37], v153 offset:40960
	ds_read_b128 v[14:17], v153 offset:43008
	v_lshl_or_b32 v2, v2, 15, v47
	v_lshl_or_b32 v2, v46, 11, v2
	v_lshl_add_u64 v[140:141], s[18:19], 0, v[2:3]
	v_lshl_add_u64 v[142:143], s[2:3], 0, v[2:3]
	s_mov_b32 s21, 0
	s_mov_b64 s[0:1], 0
	s_mov_b64 s[2:3], 0x100
	s_mov_b64 s[8:9], 0x20100
	s_mov_b64 s[16:17], 0x40100
	s_mov_b64 s[18:19], 0x60100
	v_mov_b32_e32 v2, v3
	v_mov_b32_e32 v4, v3
	v_mov_b32_e32 v5, v3
	v_mov_b32_e32 v46, v3
	v_mov_b32_e32 v47, v3
	v_mov_b32_e32 v48, v3
	v_mov_b32_e32 v49, v3
	v_mov_b32_e32 v50, v3
	v_mov_b32_e32 v51, v3
	v_mov_b32_e32 v52, v3
	v_mov_b32_e32 v53, v3
	v_mov_b32_e32 v54, v3
	v_mov_b32_e32 v55, v3
	v_mov_b32_e32 v56, v3
	v_mov_b32_e32 v57, v3
	v_mov_b32_e32 v58, v3
	v_mov_b32_e32 v59, v3
	v_mov_b32_e32 v60, v3
	v_mov_b32_e32 v61, v3
	v_mov_b32_e32 v62, v3
	v_mov_b32_e32 v63, v3
	v_mov_b32_e32 v64, v3
	v_mov_b32_e32 v65, v3
	v_mov_b32_e32 v66, v3
	v_mov_b32_e32 v67, v3
	v_mov_b32_e32 v68, v3
	v_mov_b32_e32 v69, v3
	v_mov_b32_e32 v70, v3
	v_mov_b32_e32 v71, v3
	v_mov_b32_e32 v72, v3
	v_mov_b32_e32 v73, v3
	v_mov_b32_e32 v74, v3
	v_mov_b32_e32 v75, v3
	v_mov_b32_e32 v76, v3
	v_mov_b32_e32 v77, v3
	v_mov_b32_e32 v86, v3
	v_mov_b32_e32 v87, v3
	v_mov_b32_e32 v88, v3
	v_mov_b32_e32 v89, v3
	v_mov_b32_e32 v98, v3
	v_mov_b32_e32 v99, v3
	v_mov_b32_e32 v100, v3
	v_mov_b32_e32 v101, v3
	v_mov_b32_e32 v130, v3
	v_mov_b32_e32 v131, v3
	v_mov_b32_e32 v132, v3
	v_mov_b32_e32 v133, v3
	v_mov_b32_e32 v78, v3
	v_mov_b32_e32 v79, v3
	v_mov_b32_e32 v80, v3
	v_mov_b32_e32 v81, v3
	v_mov_b32_e32 v82, v3
	v_mov_b32_e32 v83, v3
	v_mov_b32_e32 v84, v3
	v_mov_b32_e32 v85, v3
	v_mov_b32_e32 v90, v3
	v_mov_b32_e32 v91, v3
	v_mov_b32_e32 v92, v3
	v_mov_b32_e32 v93, v3
	v_mov_b32_e32 v94, v3
	v_mov_b32_e32 v95, v3
	v_mov_b32_e32 v96, v3
	v_mov_b32_e32 v97, v3
	v_mov_b32_e32 v102, v3
	v_mov_b32_e32 v103, v3
	v_mov_b32_e32 v104, v3
	v_mov_b32_e32 v105, v3
	v_mov_b32_e32 v106, v3
	v_mov_b32_e32 v107, v3
	v_mov_b32_e32 v108, v3
	v_mov_b32_e32 v109, v3
	v_mov_b32_e32 v110, v3
	v_mov_b32_e32 v111, v3
	v_mov_b32_e32 v112, v3
	v_mov_b32_e32 v113, v3
	v_mov_b32_e32 v114, v3
	v_mov_b32_e32 v115, v3
	v_mov_b32_e32 v116, v3
	v_mov_b32_e32 v117, v3
	v_mov_b32_e32 v118, v3
	v_mov_b32_e32 v119, v3
	v_mov_b32_e32 v120, v3
	v_mov_b32_e32 v121, v3
	v_mov_b32_e32 v122, v3
	v_mov_b32_e32 v123, v3
	v_mov_b32_e32 v124, v3
	v_mov_b32_e32 v125, v3
	v_mov_b32_e32 v134, v3
	v_mov_b32_e32 v135, v3
	v_mov_b32_e32 v136, v3
	v_mov_b32_e32 v137, v3
	v_mov_b32_e32 v126, v3
	v_mov_b32_e32 v127, v3
	v_mov_b32_e32 v128, v3
	v_mov_b32_e32 v129, v3
.LBB2_1:
	s_mul_i32 s22, s21, 0xe000
	v_add_u32_e32 v166, s22, v146
	v_add_u32_e32 v190, s22, v153
	s_waitcnt lgkmcnt(0)
	v_mfma_f32_16x16x32_f16 v[130:133], v[22:25], v[42:45], v[130:133]
	ds_read_b128 v[154:157], v166 offset:1024
	ds_read_b128 v[158:161], v166 offset:3072
	s_add_i32 s21, s21, 1
	v_mfma_f32_16x16x32_f16 v[98:101], v[18:21], v[42:45], v[98:101]
	ds_read_b128 v[162:165], v166 offset:5120
	ds_read_b128 v[166:169], v166 offset:7168
	v_mfma_f32_16x16x32_f16 v[86:89], v[30:33], v[42:45], v[86:89]
	ds_read_b128 v[170:173], v190 offset:33792
	ds_read_b128 v[174:177], v190 offset:35840
	v_mfma_f32_16x16x32_f16 v[74:77], v[26:29], v[42:45], v[74:77]
	ds_read_b128 v[178:181], v190 offset:37888
	ds_read_b128 v[182:185], v190 offset:39936
	v_mfma_f32_16x16x32_f16 v[70:73], v[42:45], v[34:37], v[70:73]
	ds_read_b128 v[186:189], v190 offset:41984
	ds_read_b128 v[190:193], v190 offset:44032
	v_mfma_f32_16x16x32_f16 v[66:69], v[42:45], v[14:17], v[66:69]
	v_mfma_f32_16x16x32_f16 v[62:65], v[22:25], v[38:41], v[62:65]
	v_mfma_f32_16x16x32_f16 v[58:61], v[18:21], v[38:41], v[58:61]
	v_mfma_f32_16x16x32_f16 v[54:57], v[30:33], v[38:41], v[54:57]
	v_mfma_f32_16x16x32_f16 v[50:53], v[26:29], v[38:41], v[50:53]
	v_mfma_f32_16x16x32_f16 v[46:49], v[38:41], v[34:37], v[46:49]
	v_mfma_f32_16x16x32_f16 v[2:5], v[38:41], v[14:17], v[2:5]
	v_mfma_f32_16x16x32_f16 v[78:81], v[22:25], v[10:13], v[78:81]
	v_mfma_f32_16x16x32_f16 v[82:85], v[18:21], v[10:13], v[82:85]
	v_mfma_f32_16x16x32_f16 v[90:93], v[30:33], v[10:13], v[90:93]
	v_mfma_f32_16x16x32_f16 v[94:97], v[26:29], v[10:13], v[94:97]
	v_mfma_f32_16x16x32_f16 v[102:105], v[10:13], v[34:37], v[102:105]
	v_mfma_f32_16x16x32_f16 v[106:109], v[10:13], v[14:17], v[106:109]
	v_mfma_f32_16x16x32_f16 v[110:113], v[22:25], v[6:9], v[110:113]
	v_mfma_f32_16x16x32_f16 v[114:117], v[18:21], v[6:9], v[114:117]
	v_mfma_f32_16x16x32_f16 v[118:121], v[30:33], v[6:9], v[118:121]
	v_mfma_f32_16x16x32_f16 v[122:125], v[26:29], v[6:9], v[122:125]
	v_mfma_f32_16x16x32_f16 v[134:137], v[6:9], v[34:37], v[134:137]
	v_mfma_f32_16x16x32_f16 v[126:129], v[6:9], v[14:17], v[126:129]
	v_or_b32_e32 v10, s22, v139
	v_lshl_add_u64 v[6:7], v[142:143], 0, s[0:1]
	v_readfirstlane_b32 s22, v10
	v_add_u32_e32 v11, 0x2000, v10
	v_lshl_add_u64 v[8:9], v[6:7], 0, s[2:3]
	s_mov_b32 m0, s22
	v_readfirstlane_b32 s22, v11
	v_add_u32_e32 v11, 0x4000, v10
	s_waitcnt vmcnt(0) lgkmcnt(0)
	s_barrier
	global_load_lds_dwordx4 v[8:9], off
	v_lshl_add_u64 v[8:9], v[6:7], 0, s[8:9]
	s_mov_b32 m0, s22
	v_readfirstlane_b32 s22, v11
	global_load_lds_dwordx4 v[8:9], off
	v_lshl_add_u64 v[8:9], v[6:7], 0, s[16:17]
	s_mov_b32 m0, s22
	v_lshl_add_u64 v[6:7], v[6:7], 0, s[18:19]
	global_load_lds_dwordx4 v[8:9], off
	v_add_u32_e32 v8, 0x6000, v10
	v_add_u32_e32 v11, 0x8000, v10
	v_readfirstlane_b32 s22, v8
	s_mov_b32 m0, s22
	v_readfirstlane_b32 s22, v11
	global_load_lds_dwordx4 v[6:7], off
	v_lshl_add_u64 v[6:7], v[140:141], 0, s[0:1]
	v_add_u32_e32 v11, 0xa000, v10
	v_lshl_add_u64 v[8:9], v[6:7], 0, s[2:3]
	s_mov_b32 m0, s22
	v_readfirstlane_b32 s22, v11
	global_load_lds_dwordx4 v[8:9], off
	v_lshl_add_u64 v[8:9], v[6:7], 0, s[8:9]
	s_mov_b32 m0, s22
	v_lshl_add_u64 v[6:7], v[6:7], 0, s[16:17]
	global_load_lds_dwordx4 v[8:9], off
	v_add_u32_e32 v8, 0xc000, v10
	s_cmp_lg_u32 s21, 2
	v_readfirstlane_b32 s22, v8
	s_mov_b32 m0, s22
	s_cselect_b32 s21, s21, 0
	global_load_lds_dwordx4 v[6:7], off
	s_cmpk_lt_u32 s0, 0x200
	s_cbranch_scc1 .Lmm_skip
	s_cmpk_gt_u32 s0, 0x580
	s_cbranch_scc1 .Lmm_skip
	s_cmpk_eq_u32 s0, 0x200
	s_cbranch_scc1 .Lmm_ld0
	s_cmpk_eq_u32 s0, 0x280
	s_cbranch_scc1 .Lmm_ld1
	s_cmpk_eq_u32 s0, 0x300
	s_cbranch_scc1 .Lmm_ld2
	s_cmpk_eq_u32 s0, 0x380
	s_cbranch_scc1 .Lmm_ld3
	s_cmpk_eq_u32 s0, 0x400
	s_cbranch_scc1 .Lmm_pr0
	s_cmpk_eq_u32 s0, 0x480
	s_cbranch_scc1 .Lmm_pr1
	s_cmpk_eq_u32 s0, 0x500
	s_cbranch_scc1 .Lmm_pr2
	s_cmpk_eq_u32 s0, 0x580
	s_cbranch_scc1 .Lmm_pr3
.Lmm_skip:
	s_mul_i32 s22, s21, 0xe000
	v_add_u32_e32 v6, s22, v146
	v_add_u32_e32 v14, s22, v153
	s_waitcnt lgkmcnt(0)
	v_mfma_f32_16x16x32_f16 v[130:133], v[170:173], v[154:157], v[130:133]
	ds_read_b128 v[42:45], v6
	ds_read_b128 v[38:41], v6 offset:2048
	v_mfma_f32_16x16x32_f16 v[98:101], v[174:177], v[154:157], v[98:101]
	ds_read_b128 v[10:13], v6 offset:4096
	ds_read_b128 v[6:9], v6 offset:6144
	v_mfma_f32_16x16x32_f16 v[86:89], v[178:181], v[154:157], v[86:89]
	ds_read_b128 v[22:25], v14 offset:32768
	ds_read_b128 v[18:21], v14 offset:34816
	v_mfma_f32_16x16x32_f16 v[74:77], v[182:185], v[154:157], v[74:77]
	ds_read_b128 v[30:33], v14 offset:36864
	ds_read_b128 v[26:29], v14 offset:38912
	v_mfma_f32_16x16x32_f16 v[70:73], v[154:157], v[186:189], v[70:73]
	ds_read_b128 v[34:37], v14 offset:40960
	ds_read_b128 v[14:17], v14 offset:43008
	v_mfma_f32_16x16x32_f16 v[66:69], v[154:157], v[190:193], v[66:69]
	v_mfma_f32_16x16x32_f16 v[62:65], v[170:173], v[158:161], v[62:65]
	v_mfma_f32_16x16x32_f16 v[58:61], v[174:177], v[158:161], v[58:61]
	v_mfma_f32_16x16x32_f16 v[54:57], v[178:181], v[158:161], v[54:57]
	v_mfma_f32_16x16x32_f16 v[50:53], v[182:185], v[158:161], v[50:53]
	v_mfma_f32_16x16x32_f16 v[46:49], v[158:161], v[186:189], v[46:49]
	v_mfma_f32_16x16x32_f16 v[2:5], v[158:161], v[190:193], v[2:5]
	v_mfma_f32_16x16x32_f16 v[78:81], v[170:173], v[162:165], v[78:81]
	v_mfma_f32_16x16x32_f16 v[82:85], v[174:177], v[162:165], v[82:85]
	v_mfma_f32_16x16x32_f16 v[90:93], v[178:181], v[162:165], v[90:93]
	v_mfma_f32_16x16x32_f16 v[94:97], v[182:185], v[162:165], v[94:97]
	v_mfma_f32_16x16x32_f16 v[102:105], v[162:165], v[186:189], v[102:105]
	v_mfma_f32_16x16x32_f16 v[106:109], v[162:165], v[190:193], v[106:109]
	v_mfma_f32_16x16x32_f16 v[110:113], v[170:173], v[166:169], v[110:113]
	v_mfma_f32_16x16x32_f16 v[114:117], v[174:177], v[166:169], v[114:117]
	v_mfma_f32_16x16x32_f16 v[118:121], v[178:181], v[166:169], v[118:121]
	v_mfma_f32_16x16x32_f16 v[122:125], v[182:185], v[166:169], v[122:125]
	v_mfma_f32_16x16x32_f16 v[134:137], v[166:169], v[186:189], v[134:137]
	v_mfma_f32_16x16x32_f16 v[126:129], v[166:169], v[190:193], v[126:129]
	s_add_u32 s0, s0, 0x80
	s_addc_u32 s1, s1, 0
	s_cmpk_eq_i32 s0, 0x700
	s_cbranch_scc0 .LBB2_1
	s_waitcnt lgkmcnt(0)
	v_mfma_f32_16x16x32_f16 v[130:133], v[22:25], v[42:45], v[130:133]
	ds_read_b128 v[140:143], v146 offset:1024
	ds_read_b128 v[154:157], v146 offset:3072
	v_mfma_f32_16x16x32_f16 v[98:101], v[18:21], v[42:45], v[98:101]
	ds_read_b128 v[158:161], v146 offset:5120
	ds_read_b128 v[162:165], v146 offset:7168
	v_mfma_f32_16x16x32_f16 v[86:89], v[30:33], v[42:45], v[86:89]
	ds_read_b128 v[166:169], v153 offset:33792
	ds_read_b128 v[170:173], v153 offset:35840
	v_mfma_f32_16x16x32_f16 v[74:77], v[26:29], v[42:45], v[74:77]
	ds_read_b128 v[174:177], v153 offset:37888
	ds_read_b128 v[178:181], v153 offset:39936
	v_mfma_f32_16x16x32_f16 v[70:73], v[42:45], v[34:37], v[70:73]
	ds_read_b128 v[182:185], v153 offset:41984
	ds_read_b128 v[186:189], v153 offset:44032
	v_mfma_f32_16x16x32_f16 v[42:45], v[42:45], v[14:17], v[66:69]
	v_mfma_f32_16x16x32_f16 v[62:65], v[22:25], v[38:41], v[62:65]
	v_mfma_f32_16x16x32_f16 v[58:61], v[18:21], v[38:41], v[58:61]
	v_mfma_f32_16x16x32_f16 v[54:57], v[30:33], v[38:41], v[54:57]
	v_mfma_f32_16x16x32_f16 v[50:53], v[26:29], v[38:41], v[50:53]
	v_mfma_f32_16x16x32_f16 v[46:49], v[38:41], v[34:37], v[46:49]
	v_mfma_f32_16x16x32_f16 v[2:5], v[38:41], v[14:17], v[2:5]
	v_mfma_f32_16x16x32_f16 v[38:41], v[22:25], v[10:13], v[78:81]
	v_mfma_f32_16x16x32_f16 v[66:69], v[18:21], v[10:13], v[82:85]
	v_mfma_f32_16x16x32_f16 v[78:81], v[30:33], v[10:13], v[90:93]
	v_mfma_f32_16x16x32_f16 v[82:85], v[26:29], v[10:13], v[94:97]
	v_mfma_f32_16x16x32_f16 v[90:93], v[10:13], v[34:37], v[102:105]
	v_mfma_f32_16x16x32_f16 v[94:97], v[10:13], v[14:17], v[106:109]
	v_mfma_f32_16x16x32_f16 v[22:25], v[22:25], v[6:9], v[110:113]
	v_mfma_f32_16x16x32_f16 v[102:105], v[18:21], v[6:9], v[114:117]
	v_or_b32_e32 v21, v151, v152
	v_and_b32_e32 v20, 63, v0
	v_mfma_f32_16x16x32_f16 v[30:33], v[30:33], v[6:9], v[118:121]
	v_mfma_f32_16x16x32_f16 v[26:29], v[26:29], v[6:9], v[122:125]
	v_mfma_f32_16x16x32_f16 v[34:37], v[6:9], v[34:37], v[134:137]
	v_mfma_f32_16x16x32_f16 v[6:9], v[6:9], v[14:17], v[126:129]
	v_add_u32_e32 v10, 0x16800, v21
	s_waitcnt vmcnt(0) lgkmcnt(0)
	s_waitcnt lgkmcnt(0)
	v_mfma_f32_16x16x32_f16 v[16:19], v[166:169], v[140:143], v[130:133]
	s_barrier
	ds_read_b128 v[106:109], v146 offset:57344
	ds_read_b128 v[110:113], v146 offset:59392
	v_mfma_f32_16x16x32_f16 v[98:101], v[170:173], v[140:143], v[98:101]
	ds_read_b128 v[114:117], v146 offset:61440
	ds_read_b128 v[12:15], v146 offset:63488
	v_add_u32_e32 v0, 0x16000, v21
	v_mfma_f32_16x16x32_f16 v[86:89], v[174:177], v[140:143], v[86:89]
	ds_read_b128 v[122:125], v10
	v_add_u32_e32 v10, 0x17000, v21
	ds_read_b128 v[118:121], v0
	v_mfma_f32_16x16x32_f16 v[74:77], v[178:181], v[140:143], v[74:77]
	ds_read_b128 v[126:129], v10
	v_add_u32_e32 v10, 0x17800, v21
	ds_read_b128 v[130:133], v10
	v_mfma_f32_16x16x32_f16 v[70:73], v[140:143], v[182:185], v[70:73]
	ds_read_b128 v[134:137], v0 offset:8192
	ds_read_b128 v[190:193], v0 offset:10240
	v_mfma_f32_16x16x32_f16 v[42:45], v[140:143], v[186:189], v[42:45]
	v_mfma_f32_16x16x32_f16 v[62:65], v[166:169], v[154:157], v[62:65]
	v_mfma_f32_16x16x32_f16 v[58:61], v[170:173], v[154:157], v[58:61]
	v_mfma_f32_16x16x32_f16 v[54:57], v[174:177], v[154:157], v[54:57]
	v_mfma_f32_16x16x32_f16 v[50:53], v[178:181], v[154:157], v[50:53]
	v_mfma_f32_16x16x32_f16 v[46:49], v[154:157], v[182:185], v[46:49]
	v_mfma_f32_16x16x32_f16 v[140:143], v[154:157], v[186:189], v[2:5]
	v_mfma_f32_16x16x32_f16 v[38:41], v[166:169], v[158:161], v[38:41]
	v_mfma_f32_16x16x32_f16 v[66:69], v[170:173], v[158:161], v[66:69]
	v_mfma_f32_16x16x32_f16 v[78:81], v[174:177], v[158:161], v[78:81]
	v_mfma_f32_16x16x32_f16 v[82:85], v[178:181], v[158:161], v[82:85]
	v_mfma_f32_16x16x32_f16 v[90:93], v[158:161], v[182:185], v[90:93]
	v_mfma_f32_16x16x32_f16 v[94:97], v[158:161], v[186:189], v[94:97]
	v_mfma_f32_16x16x32_f16 v[22:25], v[166:169], v[162:165], v[22:25]
	v_mfma_f32_16x16x32_f16 v[102:105], v[170:173], v[162:165], v[102:105]
	v_mfma_f32_16x16x32_f16 v[30:33], v[174:177], v[162:165], v[30:33]
	v_mfma_f32_16x16x32_f16 v[26:29], v[178:181], v[162:165], v[26:29]
	v_mfma_f32_16x16x32_f16 v[34:37], v[162:165], v[182:185], v[34:37]
	v_mfma_f32_16x16x32_f16 v[152:155], v[162:165], v[186:189], v[6:9]
	s_waitcnt lgkmcnt(0)
	v_mfma_f32_16x16x32_f16 v[156:159], v[118:121], v[106:109], v[16:19]
	s_movk_i32 s0, 0x7c0
	ds_read_b128 v[202:205], v0 offset:9216
	ds_read_b128 v[206:209], v0 offset:11264
	v_lshlrev_b32_e32 v16, 6, v144
	v_mov_b32_e32 v17, 0
	v_mov_b32_e32 v139, v17
	v_lshl_add_u64 v[4:5], s[6:7], 0, v[16:17]
	v_lshl_add_u64 v[8:9], v[4:5], 0, v[138:139]
	s_waitcnt vmcnt(0)
	v_lshlrev_b32_e32 v4, 5, v150
	v_lshl_add_u64 v[2:3], s[4:5], 0, v[16:17]
	v_ashrrev_i32_e32 v5, 31, v4
	v_lshl_add_u64 v[2:3], v[2:3], 0, v[138:139]
	v_lshlrev_b64 v[4:5], 2, v[4:5]
	v_lshl_add_u64 v[6:7], v[2:3], 0, v[4:5]
	v_lshl_add_u64 v[4:5], v[8:9], 0, v[4:5]
	v_mfma_f32_16x16x32_f16 v[98:101], v[122:125], v[106:109], v[98:101]
	global_load_dwordx4 v[160:163], v[6:7], off
	v_lshlrev_b32_e32 v18, 5, v147
	v_ashrrev_i32_e32 v19, 31, v18
	v_mfma_f32_16x16x32_f16 v[86:89], v[126:129], v[106:109], v[86:89]
	v_lshlrev_b64 v[18:19], 2, v[18:19]
	ds_read_b128 v[172:175], v146 offset:62464
	ds_read_b128 v[176:179], v146 offset:64512
	v_mfma_f32_16x16x32_f16 v[74:77], v[130:133], v[106:109], v[74:77]
	v_mfma_f32_16x16x32_f16 v[70:73], v[106:109], v[134:137], v[70:73]
	v_mfma_f32_16x16x32_f16 v[42:45], v[106:109], v[190:193], v[42:45]
	global_load_dwordx4 v[106:109], v[4:5], off
	v_lshlrev_b32_e32 v4, 5, v149
	v_ashrrev_i32_e32 v5, 31, v4
	v_lshlrev_b64 v[4:5], 2, v[4:5]
	v_lshl_add_u64 v[6:7], v[2:3], 0, v[4:5]
	v_lshl_add_u64 v[4:5], v[8:9], 0, v[4:5]
	global_load_dwordx4 v[168:171], v[4:5], off
	global_load_dwordx4 v[164:167], v[6:7], off
	v_lshlrev_b32_e32 v4, 5, v148
	v_ashrrev_i32_e32 v5, 31, v4
	v_lshlrev_b64 v[10:11], 2, v[4:5]
	v_lshl_add_u64 v[4:5], v[2:3], 0, v[10:11]
	v_lshl_add_u64 v[10:11], v[8:9], 0, v[10:11]
	global_load_dwordx4 v[210:213], v[10:11], off
	v_lshl_add_u64 v[2:3], v[2:3], 0, v[18:19]
	global_load_dwordx4 v[4:7], v[4:5], off
	v_lshl_add_u64 v[8:9], v[8:9], 0, v[18:19]
	v_add_u32_e32 v18, 0x16400, v21
	v_ashrrev_i32_e32 v10, 7, v145
	ds_read_b128 v[180:183], v18
	v_add_u32_e32 v18, 0x17400, v21
	v_and_b32_e32 v10, -16, v10
	v_add_u32_e32 v19, 0x16c00, v21
	ds_read_b128 v[194:197], v18
	v_add_u32_e32 v18, s20, v10
	global_load_dwordx4 v[8:11], v[8:9], off
	ds_read_b128 v[184:187], v19
	v_add_u32_e32 v19, 0x17c00, v21
	v_and_or_b32 v21, v145, s0, v1
	global_load_dwordx4 v[0:3], v[2:3], off
	v_mfma_f32_16x16x32_f16 v[62:65], v[118:121], v[110:113], v[62:65]
	ds_read_b128 v[198:201], v19
	v_ashrrev_i32_e32 v19, 31, v18
	ds_read_b128 v[148:151], v146 offset:60416
	v_mfma_f32_16x16x32_f16 v[58:61], v[122:125], v[110:113], v[58:61]
	v_mfma_f32_16x16x32_f16 v[54:57], v[126:129], v[110:113], v[54:57]
	v_mfma_f32_16x16x32_f16 v[50:53], v[130:133], v[110:113], v[50:53]
	v_mfma_f32_16x16x32_f16 v[46:49], v[110:113], v[134:137], v[46:49]
	v_mfma_f32_16x16x32_f16 v[110:113], v[110:113], v[190:193], v[140:143]
	s_nop 2
	ds_read_b128 v[140:143], v146 offset:58368
	v_mfma_f32_16x16x32_f16 v[38:41], v[118:121], v[114:117], v[38:41]
	v_mfma_f32_16x16x32_f16 v[66:69], v[122:125], v[114:117], v[66:69]
	v_mfma_f32_16x16x32_f16 v[78:81], v[126:129], v[114:117], v[78:81]
	v_mfma_f32_16x16x32_f16 v[82:85], v[130:133], v[114:117], v[82:85]
	v_mfma_f32_16x16x32_f16 v[90:93], v[114:117], v[134:137], v[90:93]
	v_mfma_f32_16x16x32_f16 v[94:97], v[114:117], v[190:193], v[94:97]
	s_waitcnt lgkmcnt(0)
	v_mfma_f32_16x16x32_f16 v[114:117], v[180:183], v[140:143], v[156:159]
	v_mfma_f32_16x16x32_f16 v[98:101], v[184:187], v[140:143], v[98:101]
	v_mfma_f32_16x16x32_f16 v[22:25], v[118:121], v[12:15], v[22:25]
	s_waitcnt vmcnt(6)
	s_nop 4
	v_pk_mul_f32 v[120:121], v[114:115], v[106:107] op_sel_hi:[1,0]
	v_lshlrev_b64 v[118:119], 17, v[18:19]
	v_lshl_or_b32 v118, v21, 6, v118
	v_mfma_f32_16x16x32_f16 v[102:105], v[122:125], v[12:15], v[102:105]
	v_mul_f32_e64 v122, v116, v107
	v_mul_f32_e64 v123, v117, v107
	v_pk_fma_f32 v[124:125], v[114:115], v[160:161], v[120:121] op_sel:[0,0,1] op_sel_hi:[1,1,0] neg_lo:[0,0,1] neg_hi:[0,0,1]
	v_pk_fma_f32 v[114:115], v[114:115], v[160:161], v[120:121] op_sel:[0,0,1] op_sel_hi:[1,0,0]
	v_pk_fma_f32 v[120:121], v[116:117], v[160:161], v[122:123] op_sel:[0,1,1] op_sel_hi:[1,1,0] neg_lo:[0,0,1] neg_hi:[0,0,1]
	v_pk_fma_f32 v[116:117], v[116:117], v[160:161], v[122:123] op_sel:[0,1,1] op_sel_hi:[1,1,0]
	v_cvt_pk_f16_f32 v114, v124, v115
	v_cvt_pk_f16_f32 v115, v120, v117
	v_pk_mul_f32 v[116:117], v[98:99], v[108:109] op_sel_hi:[1,0]
	v_mov_b32_e32 v122, v163
	v_pk_fma_f32 v[120:121], v[98:99], v[162:163], v[116:117] op_sel:[0,0,1] op_sel_hi:[1,1,0] neg_lo:[0,0,1] neg_hi:[0,0,1]
	v_pk_fma_f32 v[98:99], v[98:99], v[162:163], v[116:117] op_sel:[0,0,1] op_sel_hi:[1,0,0]
	v_mfma_f32_16x16x32_f16 v[30:33], v[126:129], v[12:15], v[30:33]
	v_cvt_pk_f16_f32 v116, v120, v99
	v_mov_b32_e32 v120, v109
	v_pk_mul_f32 v[98:99], v[100:101], v[120:121] op_sel_hi:[1,0]
	v_mfma_f32_16x16x32_f16 v[26:29], v[130:133], v[12:15], v[26:29]
	v_fma_f32 v124, v100, v122, -v99
	v_fma_f32 v125, v101, v122, -v98
	v_pk_fma_f32 v[98:99], v[100:101], v[122:123], v[98:99] op_sel:[0,0,1] op_sel_hi:[1,0,0]
	s_nop 0
	v_cvt_pk_f16_f32 v117, v124, v99
	v_lshlrev_b64 v[124:125], 1, v[118:119]
	v_lshl_add_u64 v[126:127], s[10:11], 0, v[124:125]
	v_mfma_f32_16x16x32_f16 v[34:37], v[12:15], v[134:137], v[34:37]
	v_mfma_f32_16x16x32_f16 v[98:101], v[12:15], v[190:193], v[152:155]
	v_lshl_add_u64 v[12:13], v[126:127], 0, v[16:17]
	v_lshl_add_u64 v[126:127], v[12:13], 0, v[138:139]
	global_store_dwordx4 v[126:127], v[114:117], off sc1
	v_mfma_f32_16x16x32_f16 v[12:15], v[194:197], v[140:143], v[86:89]
	v_mfma_f32_16x16x32_f16 v[74:77], v[198:201], v[140:143], v[74:77]
	v_mfma_f32_16x16x32_f16 v[58:61], v[184:187], v[148:151], v[58:61]
	s_nop 5
	v_mul_f32_e64 v86, v12, v106
	v_mul_f32_e64 v87, v13, v106
	v_pk_fma_f32 v[88:89], v[12:13], v[160:161], v[86:87] op_sel:[0,0,1] op_sel_hi:[1,1,0] neg_lo:[0,0,1] neg_hi:[0,0,1]
	v_pk_fma_f32 v[12:13], v[12:13], v[160:161], v[86:87] op_sel:[0,0,1] op_sel_hi:[1,0,0]
	v_mfma_f32_16x16x32_f16 v[54:57], v[194:197], v[148:151], v[54:57]
	v_cvt_pk_f16_f32 v86, v88, v13
	v_pk_mul_f32 v[12:13], v[14:15], v[106:107] op_sel:[0,1]
	s_nop 0
	v_pk_fma_f32 v[88:89], v[14:15], v[160:161], v[12:13] op_sel:[0,1,1] op_sel_hi:[1,1,0] neg_lo:[0,0,1] neg_hi:[0,0,1]
	v_pk_fma_f32 v[12:13], v[14:15], v[160:161], v[12:13] op_sel:[0,1,1] op_sel_hi:[1,1,0]
	v_mfma_f32_16x16x32_f16 v[50:53], v[198:201], v[148:151], v[50:53]
	v_cvt_pk_f16_f32 v87, v88, v13
	v_pk_mul_f32 v[88:89], v[74:75], v[108:109] op_sel_hi:[1,0]
	v_mfma_f32_16x16x32_f16 v[12:15], v[140:143], v[206:209], v[42:45]
	s_nop 2
	v_fma_f32 v42, v74, v162, -v89
	v_fma_f32 v43, v75, v163, -v88
	v_pk_fma_f32 v[44:45], v[74:75], v[162:163], v[88:89] op_sel:[0,0,1] op_sel_hi:[1,0,0]
	v_mfma_f32_16x16x32_f16 v[38:41], v[180:183], v[172:175], v[38:41]
	v_cvt_pk_f16_f32 v88, v42, v45
	v_mfma_f32_16x16x32_f16 v[42:45], v[180:183], v[148:151], v[62:65]
	s_nop 2
	v_mul_f32_e64 v62, v76, v120
	v_mul_f32_e64 v63, v77, v120
	v_mfma_f32_16x16x32_f16 v[66:69], v[184:187], v[172:175], v[66:69]
	v_fma_f32 v64, v76, v122, -v63
	v_fma_f32 v65, v77, v122, -v62
	v_pk_fma_f32 v[62:63], v[76:77], v[122:123], v[62:63] op_sel:[0,0,1] op_sel_hi:[1,0,0]
	s_nop 0
	v_cvt_pk_f16_f32 v89, v64, v63
	v_lshl_add_u64 v[62:63], s[12:13], 0, v[124:125]
	v_lshl_add_u64 v[62:63], v[62:63], 0, v[16:17]
	v_lshl_add_u64 v[106:107], v[62:63], 0, v[138:139]
	s_waitcnt vmcnt(6)
	v_pk_mul_f32 v[62:63], v[42:43], v[168:169] op_sel_hi:[1,0]
	global_store_dwordx4 v[106:107], v[86:89], off sc1
	s_waitcnt vmcnt(6)
	v_pk_fma_f32 v[64:65], v[42:43], v[164:165], v[62:63] op_sel:[0,0,1] op_sel_hi:[1,1,0] neg_lo:[0,0,1] neg_hi:[0,0,1]
	v_pk_fma_f32 v[42:43], v[42:43], v[164:165], v[62:63] op_sel:[0,0,1] op_sel_hi:[1,0,0]
	v_pk_mul_f32 v[62:63], v[44:45], v[168:169] op_sel:[0,1]
	v_cvt_pk_f16_f32 v42, v64, v43
	v_pk_fma_f32 v[74:75], v[44:45], v[164:165], v[62:63] op_sel:[0,1,1] op_sel_hi:[1,1,0] neg_lo:[0,0,1] neg_hi:[0,0,1]
	v_pk_fma_f32 v[44:45], v[44:45], v[164:165], v[62:63] op_sel:[0,1,1] op_sel_hi:[1,1,0]
	v_mov_b32_e32 v86, v171
	v_cvt_pk_f16_f32 v43, v74, v45
	v_pk_mul_f32 v[44:45], v[58:59], v[170:171] op_sel_hi:[1,0]
	v_mov_b32_e32 v88, v167
	v_pk_fma_f32 v[74:75], v[58:59], v[166:167], v[44:45] op_sel:[0,0,1] op_sel_hi:[1,1,0] neg_lo:[0,0,1] neg_hi:[0,0,1]
	v_pk_fma_f32 v[44:45], v[58:59], v[166:167], v[44:45] op_sel:[0,0,1] op_sel_hi:[1,0,0]
	v_pk_mul_f32 v[58:59], v[60:61], v[86:87] op_sel_hi:[1,0]
	v_cvt_pk_f16_f32 v44, v74, v45
	v_pk_fma_f32 v[108:109], v[60:61], v[88:89], v[58:59] op_sel:[0,0,1] op_sel_hi:[1,0,0] neg_lo:[0,0,1] neg_hi:[0,0,1]
	v_pk_fma_f32 v[58:59], v[60:61], v[88:89], v[58:59] op_sel:[0,0,1] op_sel_hi:[1,0,0]
	v_mfma_f32_16x16x32_f16 v[74:77], v[194:197], v[172:175], v[78:81]
	v_cvt_pk_f16_f32 v45, v108, v59
	global_store_dwordx4 v[126:127], v[42:45], off offset:2048 sc1
	v_pk_mul_f32 v[58:59], v[54:55], v[168:169] op_sel_hi:[1,0]
	v_mfma_f32_16x16x32_f16 v[22:25], v[180:183], v[176:179], v[22:25]
	v_fma_f32 v78, v54, v164, -v59
	v_fma_f32 v79, v55, v165, -v58
	v_pk_fma_f32 v[54:55], v[54:55], v[164:165], v[58:59] op_sel:[0,0,1] op_sel_hi:[1,0,0]
	v_mfma_f32_16x16x32_f16 v[42:45], v[198:201], v[172:175], v[82:85]
	v_cvt_pk_f16_f32 v54, v78, v55
	s_nop 1
	v_pk_mul_f32 v[82:83], v[56:57], v[168:169] op_sel:[0,1]
	v_mfma_f32_16x16x32_f16 v[30:33], v[194:197], v[176:179], v[30:33]
	v_fma_f32 v84, v56, v165, -v83
	v_fma_f32 v85, v57, v165, -v82
	v_pk_fma_f32 v[56:57], v[56:57], v[164:165], v[82:83] op_sel:[0,1,1] op_sel_hi:[1,1,0]
	s_nop 0
	v_cvt_pk_f16_f32 v55, v84, v57
	v_pk_mul_f32 v[56:57], v[50:51], v[170:171] op_sel_hi:[1,0]
	v_mfma_f32_16x16x32_f16 v[26:29], v[198:201], v[176:179], v[26:29]
	v_fma_f32 v82, v50, v166, -v57
	v_fma_f32 v83, v51, v167, -v56
	v_pk_fma_f32 v[50:51], v[50:51], v[166:167], v[56:57] op_sel:[0,0,1] op_sel_hi:[1,0,0]
	s_nop 0
	v_cvt_pk_f16_f32 v56, v82, v51
	v_pk_mul_f32 v[50:51], v[52:53], v[86:87] op_sel_hi:[1,0]
	v_mfma_f32_16x16x32_f16 v[82:85], v[184:187], v[176:179], v[102:105]
	v_fma_f32 v86, v52, v88, -v51
	v_fma_f32 v87, v53, v88, -v50
	v_pk_fma_f32 v[50:51], v[52:53], v[88:89], v[50:51] op_sel:[0,0,1] op_sel_hi:[1,0,0]
	s_nop 0
	v_cvt_pk_f16_f32 v57, v86, v51
	global_store_dwordx4 v[106:107], v[54:57], off offset:2048 sc1
	s_waitcnt vmcnt(7)
	v_pk_mul_f32 v[50:51], v[38:39], v[210:211] op_sel_hi:[1,0]
	v_mfma_f32_16x16x32_f16 v[70:73], v[140:143], v[202:205], v[70:73]
	v_mul_f32_e64 v56, v40, v211
	v_mul_f32_e64 v57, v41, v211
	s_waitcnt vmcnt(6)
	v_pk_fma_f32 v[52:53], v[38:39], v[4:5], v[50:51] op_sel:[0,0,1] op_sel_hi:[1,1,0] neg_lo:[0,0,1] neg_hi:[0,0,1]
	v_pk_fma_f32 v[38:39], v[38:39], v[4:5], v[50:51] op_sel:[0,0,1] op_sel_hi:[1,0,0]
	v_pk_fma_f32 v[86:87], v[40:41], v[4:5], v[56:57] op_sel:[0,1,1] op_sel_hi:[1,1,0] neg_lo:[0,0,1] neg_hi:[0,0,1]
	v_pk_fma_f32 v[40:41], v[40:41], v[4:5], v[56:57] op_sel:[0,1,1] op_sel_hi:[1,1,0]
	v_cvt_pk_f16_f32 v38, v52, v39
	v_cvt_pk_f16_f32 v39, v86, v41
	v_pk_mul_f32 v[40:41], v[66:67], v[212:213] op_sel_hi:[1,0]
	v_or_b32_e32 v54, 0x800, v118
	v_pk_fma_f32 v[56:57], v[66:67], v[6:7], v[40:41] op_sel:[0,0,1] op_sel_hi:[1,1,0] neg_lo:[0,0,1] neg_hi:[0,0,1]
	v_pk_fma_f32 v[40:41], v[66:67], v[6:7], v[40:41] op_sel:[0,0,1] op_sel_hi:[1,0,0]
	v_mov_b32_e32 v55, v119
	v_cvt_pk_f16_f32 v40, v56, v41
	v_mov_b32_e32 v56, v213
	v_pk_mul_f32 v[66:67], v[68:69], v[56:57] op_sel_hi:[1,0]
	v_mov_b32_e32 v86, v7
	v_pk_fma_f32 v[88:89], v[68:69], v[86:87], v[66:67] op_sel:[0,0,1] op_sel_hi:[1,0,0] neg_lo:[0,0,1] neg_hi:[0,0,1]
	v_pk_fma_f32 v[66:67], v[68:69], v[86:87], v[66:67] op_sel:[0,0,1] op_sel_hi:[1,0,0]
	v_lshlrev_b64 v[54:55], 1, v[54:55]
	v_cvt_pk_f16_f32 v41, v88, v67
	v_lshl_add_u64 v[66:67], s[10:11], 0, v[54:55]
	v_lshl_add_u64 v[66:67], v[66:67], 0, v[16:17]
	v_lshl_add_u64 v[66:67], v[66:67], 0, v[138:139]
	global_store_dwordx4 v[66:67], v[38:41], off sc1
	v_or_b32_e32 v118, 0xc00, v118
	v_mfma_f32_16x16x32_f16 v[46:49], v[148:151], v[202:205], v[46:49]
	v_mul_f32_e64 v38, v74, v210
	v_mul_f32_e64 v39, v75, v210
	v_pk_fma_f32 v[40:41], v[74:75], v[4:5], v[38:39] op_sel:[0,0,1] op_sel_hi:[1,1,0] neg_lo:[0,0,1] neg_hi:[0,0,1]
	v_pk_fma_f32 v[38:39], v[74:75], v[4:5], v[38:39] op_sel:[0,0,1] op_sel_hi:[1,0,0]
	v_mfma_f32_16x16x32_f16 v[58:61], v[172:175], v[202:205], v[90:93]
	v_cvt_pk_f16_f32 v38, v40, v39
	v_pk_mul_f32 v[40:41], v[76:77], v[210:211] op_sel:[0,1]
	s_nop 0
	v_pk_fma_f32 v[66:67], v[76:77], v[4:5], v[40:41] op_sel:[0,1,1] op_sel_hi:[1,1,0] neg_lo:[0,0,1] neg_hi:[0,0,1]
	v_pk_fma_f32 v[4:5], v[76:77], v[4:5], v[40:41] op_sel:[0,1,1] op_sel_hi:[1,1,0]
	v_mfma_f32_16x16x32_f16 v[34:37], v[176:179], v[202:205], v[34:37]
	v_cvt_pk_f16_f32 v39, v66, v5
	v_pk_mul_f32 v[4:5], v[42:43], v[212:213] op_sel_hi:[1,0]
	s_nop 0
	v_pk_fma_f32 v[40:41], v[42:43], v[6:7], v[4:5] op_sel:[0,0,1] op_sel_hi:[1,1,0] neg_lo:[0,0,1] neg_hi:[0,0,1]
	v_pk_fma_f32 v[4:5], v[42:43], v[6:7], v[4:5] op_sel:[0,0,1] op_sel_hi:[1,0,0]
	v_mfma_f32_16x16x32_f16 v[62:65], v[148:151], v[206:209], v[110:113]
	v_cvt_pk_f16_f32 v40, v40, v5
	v_pk_mul_f32 v[4:5], v[44:45], v[56:57] op_sel_hi:[1,0]
	s_nop 0
	v_pk_fma_f32 v[6:7], v[44:45], v[86:87], v[4:5] op_sel:[0,0,1] op_sel_hi:[1,0,0] neg_lo:[0,0,1] neg_hi:[0,0,1]
	v_pk_fma_f32 v[4:5], v[44:45], v[86:87], v[4:5] op_sel:[0,0,1] op_sel_hi:[1,0,0]
	v_mfma_f32_16x16x32_f16 v[78:81], v[172:175], v[206:209], v[94:97]
	v_cvt_pk_f16_f32 v41, v6, v5
	v_lshl_add_u64 v[4:5], s[12:13], 0, v[54:55]
	v_lshl_add_u64 v[4:5], v[4:5], 0, v[16:17]
	v_lshl_add_u64 v[4:5], v[4:5], 0, v[138:139]
	global_store_dwordx4 v[4:5], v[38:41], off sc1
	s_waitcnt vmcnt(7)
	v_pk_mul_f32 v[4:5], v[22:23], v[8:9] op_sel_hi:[1,0]
	v_mfma_f32_16x16x32_f16 v[50:53], v[176:179], v[206:209], v[98:101]
	s_waitcnt vmcnt(6)
	v_pk_fma_f32 v[6:7], v[22:23], v[0:1], v[4:5] op_sel:[0,0,1] op_sel_hi:[1,1,0] neg_lo:[0,0,1] neg_hi:[0,0,1]
	v_pk_fma_f32 v[4:5], v[22:23], v[0:1], v[4:5] op_sel:[0,0,1] op_sel_hi:[1,0,0]
	v_mov_b32_e32 v38, v3
	v_cvt_pk_f16_f32 v4, v6, v5
	v_pk_mul_f32 v[6:7], v[24:25], v[8:9] op_sel:[0,1]
	s_nop 0
	v_pk_fma_f32 v[22:23], v[24:25], v[0:1], v[6:7] op_sel:[0,1,1] op_sel_hi:[1,1,0] neg_lo:[0,0,1] neg_hi:[0,0,1]
	v_pk_fma_f32 v[6:7], v[24:25], v[0:1], v[6:7] op_sel:[0,1,1] op_sel_hi:[1,1,0]
	s_nop 0
	v_cvt_pk_f16_f32 v5, v22, v7
	v_pk_mul_f32 v[6:7], v[82:83], v[10:11] op_sel_hi:[1,0]
	s_nop 0
	v_pk_fma_f32 v[22:23], v[82:83], v[2:3], v[6:7] op_sel:[0,0,1] op_sel_hi:[1,1,0] neg_lo:[0,0,1] neg_hi:[0,0,1]
	v_pk_fma_f32 v[6:7], v[82:83], v[2:3], v[6:7] op_sel:[0,0,1] op_sel_hi:[1,0,0]
	s_nop 0
	v_cvt_pk_f16_f32 v6, v22, v7
	v_mov_b32_e32 v22, v11
	v_pk_mul_f32 v[24:25], v[84:85], v[22:23] op_sel_hi:[1,0]
	s_nop 0
	v_pk_fma_f32 v[40:41], v[84:85], v[38:39], v[24:25] op_sel:[0,0,1] op_sel_hi:[1,0,0] neg_lo:[0,0,1] neg_hi:[0,0,1]
	v_pk_fma_f32 v[24:25], v[84:85], v[38:39], v[24:25] op_sel:[0,0,1] op_sel_hi:[1,0,0]
	s_nop 0
	v_cvt_pk_f16_f32 v7, v40, v25
	v_lshlrev_b64 v[24:25], 1, v[118:119]
	v_lshl_add_u64 v[40:41], s[10:11], 0, v[24:25]
	v_lshl_add_u64 v[40:41], v[40:41], 0, v[16:17]
	v_lshl_add_u64 v[40:41], v[40:41], 0, v[138:139]
	global_store_dwordx4 v[40:41], v[4:7], off sc1
	s_nop 1
	v_pk_mul_f32 v[4:5], v[30:31], v[8:9] op_sel_hi:[1,0]
	s_nop 0
	v_pk_fma_f32 v[6:7], v[30:31], v[0:1], v[4:5] op_sel:[0,0,1] op_sel_hi:[1,1,0] neg_lo:[0,0,1] neg_hi:[0,0,1]
	v_pk_fma_f32 v[4:5], v[30:31], v[0:1], v[4:5] op_sel:[0,0,1] op_sel_hi:[1,0,0]
	s_nop 0
	v_cvt_pk_f16_f32 v4, v6, v5
	v_pk_mul_f32 v[6:7], v[32:33], v[8:9] op_sel:[0,1]
	s_nop 0
	v_pk_fma_f32 v[8:9], v[32:33], v[0:1], v[6:7] op_sel:[0,1,1] op_sel_hi:[1,1,0] neg_lo:[0,0,1] neg_hi:[0,0,1]
	v_pk_fma_f32 v[0:1], v[32:33], v[0:1], v[6:7] op_sel:[0,1,1] op_sel_hi:[1,1,0]
	s_nop 0
	v_cvt_pk_f16_f32 v5, v8, v1
	v_pk_mul_f32 v[0:1], v[26:27], v[10:11] op_sel_hi:[1,0]
	s_nop 0
	v_pk_fma_f32 v[6:7], v[26:27], v[2:3], v[0:1] op_sel:[0,0,1] op_sel_hi:[1,1,0] neg_lo:[0,0,1] neg_hi:[0,0,1]
	v_pk_fma_f32 v[0:1], v[26:27], v[2:3], v[0:1] op_sel:[0,0,1] op_sel_hi:[1,0,0]
	s_nop 0
	v_cvt_pk_f16_f32 v6, v6, v1
	v_pk_mul_f32 v[0:1], v[28:29], v[22:23] op_sel_hi:[1,0]
	s_nop 0
	v_pk_fma_f32 v[2:3], v[28:29], v[38:39], v[0:1] op_sel:[0,0,1] op_sel_hi:[1,0,0] neg_lo:[0,0,1] neg_hi:[0,0,1]
	v_pk_fma_f32 v[0:1], v[28:29], v[38:39], v[0:1] op_sel:[0,0,1] op_sel_hi:[1,0,0]
	v_cvt_pk_f16_f32 v3, v48, v49
	v_cvt_pk_f16_f32 v7, v2, v1
	v_lshl_add_u64 v[0:1], s[12:13], 0, v[24:25]
	v_lshl_add_u64 v[0:1], v[0:1], 0, v[16:17]
	v_lshl_add_u64 v[0:1], v[0:1], 0, v[138:139]
	global_store_dwordx4 v[0:1], v[4:7], off sc1
	v_lshlrev_b64 v[0:1], 18, v[18:19]
	v_lshlrev_b32_e32 v2, 7, v145
	v_lshl_add_u64 v[0:1], s[14:15], 0, v[0:1]
	v_and_b32_e32 v16, 0x3e000, v2
	v_lshl_add_u64 v[0:1], v[0:1], 0, v[16:17]
	v_lshlrev_b32_e32 v16, 4, v20
	v_lshl_add_u64 v[4:5], v[0:1], 0, v[16:17]
	v_lshlrev_b32_e32 v16, 12, v144
	v_cvt_pk_f16_f32 v2, v46, v47
	v_cvt_pk_f16_f32 v1, v72, v73
	v_cvt_pk_f16_f32 v0, v70, v71
	v_lshl_add_u64 v[4:5], v[4:5], 0, v[16:17]
	global_store_dwordx4 v[4:5], v[0:3], off sc1
	s_nop 1
	v_cvt_pk_f16_f32 v3, v36, v37
	v_cvt_pk_f16_f32 v2, v34, v35
	v_cvt_pk_f16_f32 v1, v60, v61
	v_cvt_pk_f16_f32 v0, v58, v59
	global_store_dwordx4 v[4:5], v[0:3], off offset:1024 sc1
	s_nop 1
	v_cvt_pk_f16_f32 v3, v64, v65
	v_cvt_pk_f16_f32 v2, v62, v63
	v_cvt_pk_f16_f32 v1, v14, v15
	v_cvt_pk_f16_f32 v0, v12, v13
	global_store_dwordx4 v[4:5], v[0:3], off offset:2048 sc1
	s_nop 1
	v_cvt_pk_f16_f32 v3, v52, v53
	v_cvt_pk_f16_f32 v2, v50, v51
	v_cvt_pk_f16_f32 v1, v80, v81
	v_cvt_pk_f16_f32 v0, v78, v79
	global_store_dwordx4 v[4:5], v[0:3], off offset:3072 sc1
	s_endpgm
.Lmm_ld0:
	global_load_dword v214, v248, s[66:67]
	v_add_u32_e32 v248, 0x2000, v248
	global_load_dword v215, v248, s[66:67]
	v_add_u32_e32 v248, 0x2000, v248
	global_load_dword v216, v248, s[66:67]
	v_add_u32_e32 v248, 0x2000, v248
	global_load_dword v217, v248, s[66:67]
	v_add_u32_e32 v248, 0x2000, v248
	global_load_dword v218, v248, s[66:67]
	v_add_u32_e32 v248, 0x2000, v248
	global_load_dword v219, v248, s[66:67]
	v_add_u32_e32 v248, 0x2000, v248
	global_load_dword v220, v248, s[66:67]
	v_add_u32_e32 v248, 0x2000, v248
	global_load_dword v221, v248, s[66:67]
	v_add_u32_e32 v248, 0x2000, v248
	s_branch .Lmm_skip
.Lmm_ld1:
	global_load_dword v222, v248, s[66:67]
	v_add_u32_e32 v248, 0x2000, v248
	global_load_dword v223, v248, s[66:67]
	v_add_u32_e32 v248, 0x2000, v248
	global_load_dword v224, v248, s[66:67]
	v_add_u32_e32 v248, 0x2000, v248
	global_load_dword v225, v248, s[66:67]
	v_add_u32_e32 v248, 0x2000, v248
	global_load_dword v226, v248, s[66:67]
	v_add_u32_e32 v248, 0x2000, v248
	global_load_dword v227, v248, s[66:67]
	v_add_u32_e32 v248, 0x2000, v248
	global_load_dword v228, v248, s[66:67]
	v_add_u32_e32 v248, 0x2000, v248
	global_load_dword v229, v248, s[66:67]
	v_add_u32_e32 v248, 0x2000, v248
	s_branch .Lmm_skip
.Lmm_ld2:
	global_load_dword v230, v248, s[66:67]
	v_add_u32_e32 v248, 0x2000, v248
	global_load_dword v231, v248, s[66:67]
	v_add_u32_e32 v248, 0x2000, v248
	global_load_dword v232, v248, s[66:67]
	v_add_u32_e32 v248, 0x2000, v248
	global_load_dword v233, v248, s[66:67]
	v_add_u32_e32 v248, 0x2000, v248
	global_load_dword v234, v248, s[66:67]
	v_add_u32_e32 v248, 0x2000, v248
	global_load_dword v235, v248, s[66:67]
	v_add_u32_e32 v248, 0x2000, v248
	global_load_dword v236, v248, s[66:67]
	v_add_u32_e32 v248, 0x2000, v248
	global_load_dword v237, v248, s[66:67]
	v_add_u32_e32 v248, 0x2000, v248
	s_branch .Lmm_skip
.Lmm_ld3:
	global_load_dword v238, v248, s[66:67]
	v_add_u32_e32 v248, 0x2000, v248
	global_load_dword v239, v248, s[66:67]
	v_add_u32_e32 v248, 0x2000, v248
	global_load_dword v240, v248, s[66:67]
	v_add_u32_e32 v248, 0x2000, v248
	global_load_dword v241, v248, s[66:67]
	v_add_u32_e32 v248, 0x2000, v248
	global_load_dword v242, v248, s[66:67]
	v_add_u32_e32 v248, 0x2000, v248
	global_load_dword v243, v248, s[66:67]
	v_add_u32_e32 v248, 0x2000, v248
	global_load_dword v244, v248, s[66:67]
	v_add_u32_e32 v248, 0x2000, v248
	global_load_dword v245, v248, s[66:67]
	v_add_u32_e32 v248, 0x2000, v248
	s_branch .Lmm_skip
.Lmm_pr0:
	v_cmp_ne_u32_e64 s[68:69], 0, v214
	v_cmp_ne_u32_e64 s[70:71], 0, v215
	s_mov_b64 s[72:73], s[68:69]
	s_mov_b64 s[74:75], s[68:69]
	v_writelane_b32 v246, s68, 0
	v_writelane_b32 v247, s69, 0
	v_cmp_ne_u32_e64 s[68:69], 0, v216
	s_or_b64 s[72:73], s[72:73], s[70:71]
	s_and_b64 s[74:75], s[74:75], s[70:71]
	v_writelane_b32 v246, s70, 1
	v_writelane_b32 v247, s71, 1
	v_cmp_ne_u32_e64 s[70:71], 0, v217
	s_or_b64 s[72:73], s[72:73], s[68:69]
	s_and_b64 s[74:75], s[74:75], s[68:69]
	v_writelane_b32 v246, s68, 2
	v_writelane_b32 v247, s69, 2
	v_cmp_ne_u32_e64 s[68:69], 0, v218
	s_or_b64 s[72:73], s[72:73], s[70:71]
	s_and_b64 s[74:75], s[74:75], s[70:71]
	v_writelane_b32 v246, s70, 3
	v_writelane_b32 v247, s71, 3
	v_cmp_ne_u32_e64 s[70:71], 0, v219
	s_or_b64 s[72:73], s[72:73], s[68:69]
	s_and_b64 s[74:75], s[74:75], s[68:69]
	v_writelane_b32 v246, s68, 4
	v_writelane_b32 v247, s69, 4
	v_cmp_ne_u32_e64 s[68:69], 0, v220
	s_or_b64 s[72:73], s[72:73], s[70:71]
	s_and_b64 s[74:75], s[74:75], s[70:71]
	v_writelane_b32 v246, s70, 5
	v_writelane_b32 v247, s71, 5
	v_cmp_ne_u32_e64 s[70:71], 0, v221
	s_or_b64 s[72:73], s[72:73], s[68:69]
	s_and_b64 s[74:75], s[74:75], s[68:69]
	v_writelane_b32 v246, s68, 6
	v_writelane_b32 v247, s69, 6
	s_nop 1
	s_or_b64 s[72:73], s[72:73], s[70:71]
	s_and_b64 s[74:75], s[74:75], s[70:71]
	v_writelane_b32 v246, s70, 7
	v_writelane_b32 v247, s71, 7
	s_branch .Lmm_skip
.Lmm_pr1:
	v_cmp_ne_u32_e64 s[68:69], 0, v222
	v_cmp_ne_u32_e64 s[70:71], 0, v223
	s_or_b64 s[72:73], s[72:73], s[68:69]
	s_and_b64 s[74:75], s[74:75], s[68:69]
	v_writelane_b32 v246, s68, 8
	v_writelane_b32 v247, s69, 8
	v_cmp_ne_u32_e64 s[68:69], 0, v224
	s_or_b64 s[72:73], s[72:73], s[70:71]
	s_and_b64 s[74:75], s[74:75], s[70:71]
	v_writelane_b32 v246, s70, 9
	v_writelane_b32 v247, s71, 9
	v_cmp_ne_u32_e64 s[70:71], 0, v225
	s_or_b64 s[72:73], s[72:73], s[68:69]
	s_and_b64 s[74:75], s[74:75], s[68:69]
	v_writelane_b32 v246, s68, 10
	v_writelane_b32 v247, s69, 10
	v_cmp_ne_u32_e64 s[68:69], 0, v226
	s_or_b64 s[72:73], s[72:73], s[70:71]
	s_and_b64 s[74:75], s[74:75], s[70:71]
	v_writelane_b32 v246, s70, 11
	v_writelane_b32 v247, s71, 11
	v_cmp_ne_u32_e64 s[70:71], 0, v227
	s_or_b64 s[72:73], s[72:73], s[68:69]
	s_and_b64 s[74:75], s[74:75], s[68:69]
	v_writelane_b32 v246, s68, 12
	v_writelane_b32 v247, s69, 12
	v_cmp_ne_u32_e64 s[68:69], 0, v228
	s_or_b64 s[72:73], s[72:73], s[70:71]
	s_and_b64 s[74:75], s[74:75], s[70:71]
	v_writelane_b32 v246, s70, 13
	v_writelane_b32 v247, s71, 13
	v_cmp_ne_u32_e64 s[70:71], 0, v229
	s_or_b64 s[72:73], s[72:73], s[68:69]
	s_and_b64 s[74:75], s[74:75], s[68:69]
	v_writelane_b32 v246, s68, 14
	v_writelane_b32 v247, s69, 14
	s_nop 1
	s_or_b64 s[72:73], s[72:73], s[70:71]
	s_and_b64 s[74:75], s[74:75], s[70:71]
	v_writelane_b32 v246, s70, 15
	v_writelane_b32 v247, s71, 15
	s_cmp_lg_u64 s[72:73], 0
	s_cselect_b32 s76, 1, 0
	s_cmp_eq_u64 s[74:75], -1
	s_cselect_b32 s78, 2, 0
	s_lshr_b64 s[80:81], s[72:73], 16
	s_cmp_eq_u64 s[80:81], 0
	s_cselect_b32 s79, 4, 0
	s_or_b32 s76, s76, s78
	s_or_b32 s76, s76, s79
	s_branch .Lmm_skip
.Lmm_pr2:
	v_cmp_ne_u32_e64 s[68:69], 0, v230
	v_cmp_ne_u32_e64 s[70:71], 0, v231
	s_mov_b64 s[72:73], s[68:69]
	s_mov_b64 s[74:75], s[68:69]
	v_writelane_b32 v246, s68, 16
	v_writelane_b32 v247, s69, 16
	v_cmp_ne_u32_e64 s[68:69], 0, v232
	s_or_b64 s[72:73], s[72:73], s[70:71]
	s_and_b64 s[74:75], s[74:75], s[70:71]
	v_writelane_b32 v246, s70, 17
	v_writelane_b32 v247, s71, 17
	v_cmp_ne_u32_e64 s[70:71], 0, v233
	s_or_b64 s[72:73], s[72:73], s[68:69]
	s_and_b64 s[74:75], s[74:75], s[68:69]
	v_writelane_b32 v246, s68, 18
	v_writelane_b32 v247, s69, 18
	v_cmp_ne_u32_e64 s[68:69], 0, v234
	s_or_b64 s[72:73], s[72:73], s[70:71]
	s_and_b64 s[74:75], s[74:75], s[70:71]
	v_writelane_b32 v246, s70, 19
	v_writelane_b32 v247, s71, 19
	v_cmp_ne_u32_e64 s[70:71], 0, v235
	s_or_b64 s[72:73], s[72:73], s[68:69]
	s_and_b64 s[74:75], s[74:75], s[68:69]
	v_writelane_b32 v246, s68, 20
	v_writelane_b32 v247, s69, 20
	v_cmp_ne_u32_e64 s[68:69], 0, v236
	s_or_b64 s[72:73], s[72:73], s[70:71]
	s_and_b64 s[74:75], s[74:75], s[70:71]
	v_writelane_b32 v246, s70, 21
	v_writelane_b32 v247, s71, 21
	v_cmp_ne_u32_e64 s[70:71], 0, v237
	s_or_b64 s[72:73], s[72:73], s[68:69]
	s_and_b64 s[74:75], s[74:75], s[68:69]
	v_writelane_b32 v246, s68, 22
	v_writelane_b32 v247, s69, 22
	s_nop 1
	s_or_b64 s[72:73], s[72:73], s[70:71]
	s_and_b64 s[74:75], s[74:75], s[70:71]
	v_writelane_b32 v246, s70, 23
	v_writelane_b32 v247, s71, 23
	s_branch .Lmm_skip
.Lmm_pr3:
	v_cmp_ne_u32_e64 s[68:69], 0, v238
	v_cmp_ne_u32_e64 s[70:71], 0, v239
	s_or_b64 s[72:73], s[72:73], s[68:69]
	s_and_b64 s[74:75], s[74:75], s[68:69]
	v_writelane_b32 v246, s68, 24
	v_writelane_b32 v247, s69, 24
	v_cmp_ne_u32_e64 s[68:69], 0, v240
	s_or_b64 s[72:73], s[72:73], s[70:71]
	s_and_b64 s[74:75], s[74:75], s[70:71]
	v_writelane_b32 v246, s70, 25
	v_writelane_b32 v247, s71, 25
	v_cmp_ne_u32_e64 s[70:71], 0, v241
	s_or_b64 s[72:73], s[72:73], s[68:69]
	s_and_b64 s[74:75], s[74:75], s[68:69]
	v_writelane_b32 v246, s68, 26
	v_writelane_b32 v247, s69, 26
	v_cmp_ne_u32_e64 s[68:69], 0, v242
	s_or_b64 s[72:73], s[72:73], s[70:71]
	s_and_b64 s[74:75], s[74:75], s[70:71]
	v_writelane_b32 v246, s70, 27
	v_writelane_b32 v247, s71, 27
	v_cmp_ne_u32_e64 s[70:71], 0, v243
	s_or_b64 s[72:73], s[72:73], s[68:69]
	s_and_b64 s[74:75], s[74:75], s[68:69]
	v_writelane_b32 v246, s68, 28
	v_writelane_b32 v247, s69, 28
	v_cmp_ne_u32_e64 s[68:69], 0, v244
	s_or_b64 s[72:73], s[72:73], s[70:71]
	s_and_b64 s[74:75], s[74:75], s[70:71]
	v_writelane_b32 v246, s70, 29
	v_writelane_b32 v247, s71, 29
	v_cmp_ne_u32_e64 s[70:71], 0, v245
	s_or_b64 s[72:73], s[72:73], s[68:69]
	s_and_b64 s[74:75], s[74:75], s[68:69]
	v_writelane_b32 v246, s68, 30
	v_writelane_b32 v247, s69, 30
	s_nop 1
	s_or_b64 s[72:73], s[72:73], s[70:71]
	s_and_b64 s[74:75], s[74:75], s[70:71]
	v_writelane_b32 v246, s70, 31
	v_writelane_b32 v247, s71, 31
	s_cmp_lg_u64 s[72:73], 0
	s_cselect_b32 s77, 1, 0
	s_cmp_eq_u64 s[74:75], -1
	s_cselect_b32 s78, 2, 0
	s_lshr_b64 s[80:81], s[72:73], 16
	s_cmp_eq_u64 s[80:81], 0
	s_cselect_b32 s79, 4, 0
	s_or_b32 s77, s77, s78
	s_or_b32 s77, s77, s79
	v_and_b32_e32 v248, 63, v0
	v_lshlrev_b32_e32 v248, 3, v248
	s_lshl_b32 s84, s59, 11
	s_add_u32 s84, s84, s58
	s_lshl_b32 s84, s84, 3
	s_add_u32 s82, s54, s84
	s_addc_u32 s83, s55, 0
	v_mov_b32_e32 v249, s76
	v_mov_b32_e32 v251, s77
	v_mov_b32_e32 v250, s60
	v_add_u32_e32 v252, 1, v250
	s_mov_b32 exec_hi, 0
	global_store_dwordx2 v248, v[246:247], s[82:83]
	s_mov_b32 exec_lo, 1
	global_store_byte v250, v249, s[56:57]
	global_store_byte v252, v251, s[56:57]
	s_mov_b64 exec, -1
	s_nop 4
	s_branch .Lmm_skip
	.p2align	8
